# v36
# speedup vs baseline: 1.0093x; 1.0062x over previous
_Z10lstm_fusedPKfS0_S0_S0_S0_S0_S0_S0_S0_S0_S0_Pf:
	s_load_dwordx16 s[36:51], s[0:1], 0x0
	s_load_dwordx8 s[52:59], s[0:1], 0x40
	s_load_dword s21, s[0:1], 0x60
	v_readfirstlane_b32 s3, v0
	v_and_b32_e32 v69, 63, v0
	v_and_b32_e32 v68, 15, v0
	v_bfe_u32 v1, v0, 4, 2
	s_lshr_b32 s3, s3, 6
	s_mov_b32 s35, s3
	s_add_u32 s27, s3, s2
	s_and_b32 s27, s27, 15
	s_lshl_b32 s28, s27, 10
	s_lshl_b32 s29, s27, 6
	s_lshl_b32 s2, s2, 4
	s_add_i32 s20, s3, s2
	v_lshlrev_b32_e32 v2, 5, v1
	v_mov_b32_e32 v3, 0
	v_lshl_add_u32 v60, v69, 4, s28
	s_lshl_b32 s26, s20, 12
	s_waitcnt lgkmcnt(0)
	s_load_dword s34, s[56:57], 0x0
	v_lshl_add_u64 v[42:43], s[36:37], 0, v[2:3]
	v_lshl_or_b32 v2, v68, 7, s26
	v_lshl_add_u64 v[74:75], v[42:43], 0, v[2:3]
	s_cmp_lt_u32 s35, 4
	s_cbranch_scc0 .Lpx_lead_skip
	global_load_dwordx4 v[10:13], v[74:75], off offset:16 nt
	global_load_dwordx4 v[14:17], v[74:75], off nt
	global_load_dwordx4 v[2:5], v[74:75], off offset:2064 nt
	global_load_dwordx4 v[6:9], v[74:75], off offset:2048 nt
.Lpx_lead_skip:
	s_add_u32 s4, s27, 0
	s_mov_b32 s24, 0
	s_mov_b32 s25, 0
	s_sub_u32 s5, s4, 12
	s_mov_b64 s[8:9], s[44:45]
	s_movk_i32 s10, 0x100
	s_movk_i32 s11, 16
	s_movk_i32 s12, 64
	s_mov_b32 s13, 0xbf2562dd
	s_mov_b32 s14, 0xbfa562dd
	s_mov_b32 s15, 1
	s_cmp_lt_u32 s4, 12
	s_cbranch_scc0 .Lpr0_cls
	s_lshl_b32 s5, s4, 1
	s_mov_b64 s[8:9], s[38:39]
	s_movk_i32 s10, 0x80
	s_movk_i32 s11, 32
	s_movk_i32 s12, 16
	s_mov_b32 s13, 0xbfb8aa3b
	s_mov_b32 s14, 0xc038aa3b

.Lpb_skip:
	s_cmp_lt_u32 s35, 4
	s_cbranch_scc1 .Lpx_fol_skip
	global_load_dwordx4 v[10:13], v[74:75], off offset:16 nt
	global_load_dwordx4 v[14:17], v[74:75], off nt
	global_load_dwordx4 v[2:5], v[74:75], off offset:2064 nt
	global_load_dwordx4 v[6:9], v[74:75], off offset:2048 nt
.Lpx_fol_skip:
	s_cmp_lt_u32 s35, 4
	s_cbranch_scc1 .Lpw_lead0
	s_waitcnt vmcnt(8)
	s_branch .Lpw_done0

.Lpw_done0:
	v_pk_mul_f32 v[18:19], v[18:19], v[48:49] op_sel_hi:[1,0]
	v_pk_mul_f32 v[20:21], v[20:21], v[48:49] op_sel_hi:[1,0]
	v_pk_mul_f32 v[22:23], v[22:23], v[48:49] op_sel_hi:[1,0]
	v_pk_mul_f32 v[24:25], v[24:25], v[48:49] op_sel_hi:[1,0]
	v_cvt_pk_f16_f32 v18, v18, v19
	v_cvt_pk_f16_f32 v19, v20, v21
	v_cvt_pk_f16_f32 v20, v22, v23
	v_cvt_pk_f16_f32 v21, v24, v25
	ds_write_b128 v60, v[18:21]
	s_cmp_lt_u32 s35, 4
	s_cbranch_scc1 .Lpw_lead1
	s_waitcnt vmcnt(6)
	s_branch .Lpw_done1
.Lpw_lead1:
	s_waitcnt vmcnt(2)
.Lpw_done1:
	v_pk_mul_f32 v[26:27], v[26:27], v[50:51] op_sel_hi:[1,0]
	v_pk_mul_f32 v[28:29], v[28:29], v[50:51] op_sel_hi:[1,0]
	v_pk_mul_f32 v[30:31], v[30:31], v[50:51] op_sel_hi:[1,0]
	v_pk_mul_f32 v[32:33], v[32:33], v[50:51] op_sel_hi:[1,0]
	v_cvt_pk_f16_f32 v26, v26, v27
	v_cvt_pk_f16_f32 v27, v28, v29
	v_cvt_pk_f16_f32 v28, v30, v31
	v_cvt_pk_f16_f32 v29, v32, v33
	ds_write_b128 v60, v[26:29] offset:16384
	s_cmp_lt_u32 s35, 4
	s_cbranch_scc1 .Lpw_lead2
	s_waitcnt vmcnt(4)
	s_branch .Lpw_done2
.Lpw_lead2:
	s_waitcnt vmcnt(0)
